# v1
# speedup vs baseline: 1.0094x; 1.0094x over previous
.LBB0_17:
	s_ashr_i32 s27, s35, 5
	s_cmp_eq_u32 s27, s34
	s_cbranch_scc1 .LBB0_37
	ds_bpermute_b32 v98, v208, v218
	v_max_f32_e32 v99, v218, v218
	v_mov_b32_e32 v101, 0
	v_mov_b32_e32 v102, 0
	v_mov_b32_e32 v103, 0
	s_waitcnt lgkmcnt(0)
	v_max_f32_e32 v98, v98, v98
	v_max_f32_e32 v98, v99, v98
	ds_bpermute_b32 v99, v207, v98
	v_mov_b32_e32 v104, 0
	v_mov_b32_e32 v105, 0
	v_mov_b32_e32 v106, 0
	s_lshl_b32 s24, s34, 3
	s_waitcnt lgkmcnt(0)
	v_max_f32_e32 v99, v99, v99
	v_max_f32_e32 v98, v98, v99
	ds_bpermute_b32 v100, v206, v98
	s_add_i32 s24, s24, s31
	s_mul_i32 s28, s24, 0x210
	v_mov_b32_e32 v99, 0
	s_add_i32 s28, s28, 0x23440
	s_waitcnt lgkmcnt(0)
	v_max_f32_e32 v100, v100, v100
	v_max_f32_e32 v98, v98, v100
	ds_bpermute_b32 v100, v205, v98
	v_add_u32_e32 v111, s28, v203
	s_waitcnt lgkmcnt(0)
	v_max_f32_e32 v100, v100, v100
	v_max_f32_e32 v98, v98, v100
	v_sub_f32_e32 v100, v218, v98
	v_exp_f32_e32 v100, v100
	s_nop 0
	v_mul_f32_e32 v107, v219, v100
	v_pk_mul_f32 v[108:109], v[100:101], v[198:199] op_sel_hi:[0,1]
	s_nop 0
	v_mov_b32_dpp v101, v107 row_shr:1 row_mask:0xf bank_mask:0xf
	v_fmac_f32_e32 v101, v219, v100
	v_mov_b32_dpp v102, v108 row_shr:1 row_mask:0xf bank_mask:0xf
	v_mov_b32_dpp v103, v109 row_shr:1 row_mask:0xf bank_mask:0xf
	v_pk_fma_f32 v[102:103], v[100:101], v[198:199], v[102:103] op_sel_hi:[0,1,1]
	v_mov_b32_e32 v107, 0
	v_add_f32_dpp v101, v101, v101 row_shr:2 row_mask:0xf bank_mask:0xf bound_ctrl:1
	v_mov_b32_dpp v104, v102 row_shr:2 row_mask:0xf bank_mask:0xf
	v_mov_b32_dpp v105, v103 row_shr:2 row_mask:0xf bank_mask:0xf
	v_pk_add_f32 v[102:103], v[102:103], v[104:105]
	v_mov_b32_e32 v108, 0
	v_mov_b32_e32 v109, 0
	v_mov_b32_dpp v106, v102 row_shr:4 row_mask:0xf bank_mask:0xf
	v_mov_b32_dpp v107, v103 row_shr:4 row_mask:0xf bank_mask:0xf
	v_pk_add_f32 v[102:103], v[102:103], v[106:107]
	v_pk_mul_f32 v[106:107], v[100:101], v[196:197] op_sel_hi:[0,1]
	v_add_f32_dpp v110, v101, v101 row_shr:4 row_mask:0xf bank_mask:0xf bound_ctrl:1
	v_mov_b32_e32 v104, 0
	v_mov_b32_dpp v108, v106 row_shr:1 row_mask:0xf bank_mask:0xf
	v_mov_b32_dpp v109, v107 row_shr:1 row_mask:0xf bank_mask:0xf
	v_pk_fma_f32 v[106:107], v[100:101], v[196:197], v[108:109] op_sel_hi:[0,1,1]
	v_mov_b32_e32 v108, 0
	v_mov_b32_e32 v109, 0
	v_mov_b32_e32 v105, 0
	v_mov_b32_dpp v108, v106 row_shr:2 row_mask:0xf bank_mask:0xf
	v_mov_b32_dpp v109, v107 row_shr:2 row_mask:0xf bank_mask:0xf
	v_pk_add_f32 v[106:107], v[106:107], v[108:109]
	v_mov_b32_e32 v108, 0
	v_mov_b32_e32 v109, 0
	v_mov_b32_dpp v99, v110 row_shr:8 row_mask:0xf bank_mask:0xf
	v_mov_b32_dpp v108, v106 row_shr:4 row_mask:0xf bank_mask:0xf
	v_mov_b32_dpp v109, v107 row_shr:4 row_mask:0xf bank_mask:0xf
	v_pk_add_f32 v[106:107], v[106:107], v[108:109]
	v_mov_b32_e32 v108, 0
	v_mov_b32_e32 v109, 0
	v_mov_b32_dpp v104, v102 row_shr:8 row_mask:0xf bank_mask:0xf
	v_mov_b32_dpp v105, v103 row_shr:8 row_mask:0xf bank_mask:0xf
	v_mov_b32_dpp v108, v106 row_shr:8 row_mask:0xf bank_mask:0xf
	v_mov_b32_dpp v109, v107 row_shr:8 row_mask:0xf bank_mask:0xf
	s_and_saveexec_b64 s[24:25], s[6:7]
	v_pk_add_f32 v[106:107], v[106:107], v[108:109]
	v_pk_add_f32 v[104:105], v[102:103], v[104:105]
	ds_write_b128 v111, v[104:107]
	s_or_b64 exec, exec, s[24:25]
	v_mov_b32_e32 v101, v100
	v_pk_mul_f32 v[102:103], v[100:101], v[194:195]
	v_mov_b32_e32 v104, 0
	v_mov_b32_e32 v105, 0
	v_pk_mul_f32 v[106:107], v[100:101], v[192:193]
	v_mov_b32_e32 v108, 0
	v_mov_b32_e32 v109, 0
	v_mov_b32_dpp v104, v102 row_shr:1 row_mask:0xf bank_mask:0xf
	v_mov_b32_dpp v105, v103 row_shr:1 row_mask:0xf bank_mask:0xf
	v_mov_b32_dpp v108, v106 row_shr:1 row_mask:0xf bank_mask:0xf
	v_mov_b32_dpp v109, v107 row_shr:1 row_mask:0xf bank_mask:0xf
	v_pk_fma_f32 v[102:103], v[100:101], v[194:195], v[104:105]
	v_mov_b32_e32 v104, 0
	v_mov_b32_e32 v105, 0
	v_pk_fma_f32 v[106:107], v[100:101], v[192:193], v[108:109]
	v_mov_b32_e32 v108, 0
	v_mov_b32_e32 v109, 0
	v_mov_b32_dpp v104, v102 row_shr:2 row_mask:0xf bank_mask:0xf
	v_mov_b32_dpp v105, v103 row_shr:2 row_mask:0xf bank_mask:0xf
	v_mov_b32_dpp v108, v106 row_shr:2 row_mask:0xf bank_mask:0xf
	v_mov_b32_dpp v109, v107 row_shr:2 row_mask:0xf bank_mask:0xf
	v_pk_add_f32 v[102:103], v[102:103], v[104:105]
	v_mov_b32_e32 v104, 0
	v_mov_b32_e32 v105, 0
	v_pk_add_f32 v[106:107], v[106:107], v[108:109]
	v_mov_b32_e32 v108, 0
	v_mov_b32_e32 v109, 0
	v_mov_b32_dpp v104, v102 row_shr:4 row_mask:0xf bank_mask:0xf
	v_mov_b32_dpp v105, v103 row_shr:4 row_mask:0xf bank_mask:0xf
	v_mov_b32_dpp v108, v106 row_shr:4 row_mask:0xf bank_mask:0xf
	v_mov_b32_dpp v109, v107 row_shr:4 row_mask:0xf bank_mask:0xf
	v_pk_add_f32 v[102:103], v[102:103], v[104:105]
	v_mov_b32_e32 v104, 0
	v_mov_b32_e32 v105, 0
	v_pk_add_f32 v[106:107], v[106:107], v[108:109]
	v_mov_b32_e32 v108, 0
	v_mov_b32_e32 v109, 0
	v_mov_b32_dpp v104, v102 row_shr:8 row_mask:0xf bank_mask:0xf
	v_mov_b32_dpp v105, v103 row_shr:8 row_mask:0xf bank_mask:0xf
	v_mov_b32_dpp v108, v106 row_shr:8 row_mask:0xf bank_mask:0xf
	v_mov_b32_dpp v109, v107 row_shr:8 row_mask:0xf bank_mask:0xf
	s_and_saveexec_b64 s[24:25], s[6:7]
	v_pk_add_f32 v[106:107], v[106:107], v[108:109]
	v_pk_add_f32 v[104:105], v[102:103], v[104:105]
	ds_write_b128 v111, v[104:107] offset:64
	s_or_b64 exec, exec, s[24:25]
	v_pk_mul_f32 v[102:103], v[100:101], v[190:191]
	v_mov_b32_e32 v104, 0
	v_mov_b32_e32 v105, 0
	v_pk_mul_f32 v[106:107], v[100:101], v[188:189]
	v_mov_b32_e32 v108, 0
	v_mov_b32_e32 v109, 0
	v_mov_b32_dpp v104, v102 row_shr:1 row_mask:0xf bank_mask:0xf
	v_mov_b32_dpp v105, v103 row_shr:1 row_mask:0xf bank_mask:0xf
	v_mov_b32_dpp v108, v106 row_shr:1 row_mask:0xf bank_mask:0xf
	v_mov_b32_dpp v109, v107 row_shr:1 row_mask:0xf bank_mask:0xf
	v_pk_fma_f32 v[102:103], v[100:101], v[190:191], v[104:105]
	v_mov_b32_e32 v104, 0
	v_mov_b32_e32 v105, 0
	v_pk_fma_f32 v[106:107], v[100:101], v[188:189], v[108:109]
	v_mov_b32_e32 v108, 0
	v_mov_b32_e32 v109, 0
	v_mov_b32_dpp v104, v102 row_shr:2 row_mask:0xf bank_mask:0xf
	v_mov_b32_dpp v105, v103 row_shr:2 row_mask:0xf bank_mask:0xf
	v_mov_b32_dpp v108, v106 row_shr:2 row_mask:0xf bank_mask:0xf
	v_mov_b32_dpp v109, v107 row_shr:2 row_mask:0xf bank_mask:0xf
	v_pk_add_f32 v[102:103], v[102:103], v[104:105]
	v_mov_b32_e32 v104, 0
	v_mov_b32_e32 v105, 0
	v_pk_add_f32 v[106:107], v[106:107], v[108:109]
	v_mov_b32_e32 v108, 0
	v_mov_b32_e32 v109, 0
	v_mov_b32_dpp v104, v102 row_shr:4 row_mask:0xf bank_mask:0xf
	v_mov_b32_dpp v105, v103 row_shr:4 row_mask:0xf bank_mask:0xf
	v_mov_b32_dpp v108, v106 row_shr:4 row_mask:0xf bank_mask:0xf
	v_mov_b32_dpp v109, v107 row_shr:4 row_mask:0xf bank_mask:0xf
	v_pk_add_f32 v[102:103], v[102:103], v[104:105]
	v_mov_b32_e32 v104, 0
	v_mov_b32_e32 v105, 0
	v_pk_add_f32 v[106:107], v[106:107], v[108:109]
	v_mov_b32_e32 v108, 0
	v_mov_b32_e32 v109, 0
	v_mov_b32_dpp v104, v102 row_shr:8 row_mask:0xf bank_mask:0xf
	v_mov_b32_dpp v105, v103 row_shr:8 row_mask:0xf bank_mask:0xf
	v_mov_b32_dpp v108, v106 row_shr:8 row_mask:0xf bank_mask:0xf
	v_mov_b32_dpp v109, v107 row_shr:8 row_mask:0xf bank_mask:0xf
	s_and_saveexec_b64 s[24:25], s[6:7]
	v_pk_add_f32 v[106:107], v[106:107], v[108:109]
	v_pk_add_f32 v[104:105], v[102:103], v[104:105]
	ds_write_b128 v111, v[104:107] offset:128
	s_or_b64 exec, exec, s[24:25]
	v_pk_mul_f32 v[102:103], v[100:101], v[186:187]
	v_mov_b32_e32 v104, 0
	v_mov_b32_e32 v105, 0
	v_pk_mul_f32 v[106:107], v[100:101], v[184:185]
	v_mov_b32_e32 v108, 0
	v_mov_b32_e32 v109, 0
	v_mov_b32_dpp v104, v102 row_shr:1 row_mask:0xf bank_mask:0xf
	v_mov_b32_dpp v105, v103 row_shr:1 row_mask:0xf bank_mask:0xf
	v_mov_b32_dpp v108, v106 row_shr:1 row_mask:0xf bank_mask:0xf
	v_mov_b32_dpp v109, v107 row_shr:1 row_mask:0xf bank_mask:0xf
	v_pk_fma_f32 v[102:103], v[100:101], v[186:187], v[104:105]
	v_mov_b32_e32 v104, 0
	v_mov_b32_e32 v105, 0
	v_pk_fma_f32 v[106:107], v[100:101], v[184:185], v[108:109]
	v_mov_b32_e32 v108, 0
	v_mov_b32_e32 v109, 0
	v_mov_b32_dpp v104, v102 row_shr:2 row_mask:0xf bank_mask:0xf
	v_mov_b32_dpp v105, v103 row_shr:2 row_mask:0xf bank_mask:0xf
	v_mov_b32_dpp v108, v106 row_shr:2 row_mask:0xf bank_mask:0xf
	v_mov_b32_dpp v109, v107 row_shr:2 row_mask:0xf bank_mask:0xf
	v_pk_add_f32 v[102:103], v[102:103], v[104:105]
	v_mov_b32_e32 v104, 0
	v_mov_b32_e32 v105, 0
	v_pk_add_f32 v[106:107], v[106:107], v[108:109]
	v_mov_b32_e32 v108, 0
	v_mov_b32_e32 v109, 0
	v_mov_b32_dpp v104, v102 row_shr:4 row_mask:0xf bank_mask:0xf
	v_mov_b32_dpp v105, v103 row_shr:4 row_mask:0xf bank_mask:0xf
	v_mov_b32_dpp v108, v106 row_shr:4 row_mask:0xf bank_mask:0xf
	v_mov_b32_dpp v109, v107 row_shr:4 row_mask:0xf bank_mask:0xf
	v_pk_add_f32 v[102:103], v[102:103], v[104:105]
	v_mov_b32_e32 v104, 0
	v_mov_b32_e32 v105, 0
	v_pk_add_f32 v[106:107], v[106:107], v[108:109]
	v_mov_b32_e32 v108, 0
	v_mov_b32_e32 v109, 0
	v_mov_b32_dpp v104, v102 row_shr:8 row_mask:0xf bank_mask:0xf
	v_mov_b32_dpp v105, v103 row_shr:8 row_mask:0xf bank_mask:0xf
	v_mov_b32_dpp v108, v106 row_shr:8 row_mask:0xf bank_mask:0xf
	v_mov_b32_dpp v109, v107 row_shr:8 row_mask:0xf bank_mask:0xf
	s_and_saveexec_b64 s[24:25], s[6:7]
	v_pk_add_f32 v[106:107], v[106:107], v[108:109]
	v_pk_add_f32 v[104:105], v[102:103], v[104:105]
	ds_write_b128 v111, v[104:107] offset:192
	s_or_b64 exec, exec, s[24:25]
	v_pk_mul_f32 v[102:103], v[100:101], v[182:183]
	v_mov_b32_e32 v104, 0
	v_mov_b32_e32 v105, 0
	v_pk_mul_f32 v[106:107], v[100:101], v[180:181]
	v_mov_b32_e32 v108, 0
	v_mov_b32_e32 v109, 0
	v_mov_b32_dpp v104, v102 row_shr:1 row_mask:0xf bank_mask:0xf
	v_mov_b32_dpp v105, v103 row_shr:1 row_mask:0xf bank_mask:0xf
	v_mov_b32_dpp v108, v106 row_shr:1 row_mask:0xf bank_mask:0xf
	v_mov_b32_dpp v109, v107 row_shr:1 row_mask:0xf bank_mask:0xf
	v_pk_fma_f32 v[102:103], v[100:101], v[182:183], v[104:105]
	v_mov_b32_e32 v104, 0
	v_mov_b32_e32 v105, 0
	v_pk_fma_f32 v[106:107], v[100:101], v[180:181], v[108:109]
	v_mov_b32_e32 v108, 0
	v_mov_b32_e32 v109, 0
	v_mov_b32_dpp v104, v102 row_shr:2 row_mask:0xf bank_mask:0xf
	v_mov_b32_dpp v105, v103 row_shr:2 row_mask:0xf bank_mask:0xf
	v_mov_b32_dpp v108, v106 row_shr:2 row_mask:0xf bank_mask:0xf
	v_mov_b32_dpp v109, v107 row_shr:2 row_mask:0xf bank_mask:0xf
	v_pk_add_f32 v[102:103], v[102:103], v[104:105]
	v_mov_b32_e32 v104, 0
	v_mov_b32_e32 v105, 0
	v_pk_add_f32 v[106:107], v[106:107], v[108:109]
	v_mov_b32_e32 v108, 0
	v_mov_b32_e32 v109, 0
	v_mov_b32_dpp v104, v102 row_shr:4 row_mask:0xf bank_mask:0xf
	v_mov_b32_dpp v105, v103 row_shr:4 row_mask:0xf bank_mask:0xf
	v_mov_b32_dpp v108, v106 row_shr:4 row_mask:0xf bank_mask:0xf
	v_mov_b32_dpp v109, v107 row_shr:4 row_mask:0xf bank_mask:0xf
	v_pk_add_f32 v[102:103], v[102:103], v[104:105]
	v_mov_b32_e32 v104, 0
	v_mov_b32_e32 v105, 0
	v_pk_add_f32 v[106:107], v[106:107], v[108:109]
	v_mov_b32_e32 v108, 0
	v_mov_b32_e32 v109, 0
	v_mov_b32_dpp v104, v102 row_shr:8 row_mask:0xf bank_mask:0xf
	v_mov_b32_dpp v105, v103 row_shr:8 row_mask:0xf bank_mask:0xf
	v_mov_b32_dpp v108, v106 row_shr:8 row_mask:0xf bank_mask:0xf
	v_mov_b32_dpp v109, v107 row_shr:8 row_mask:0xf bank_mask:0xf
	s_and_saveexec_b64 s[24:25], s[6:7]
	v_pk_add_f32 v[106:107], v[106:107], v[108:109]
	v_pk_add_f32 v[104:105], v[102:103], v[104:105]
	ds_write_b128 v111, v[104:107] offset:256
	s_or_b64 exec, exec, s[24:25]
	v_pk_mul_f32 v[102:103], v[100:101], v[178:179]
	v_mov_b32_e32 v104, 0
	v_mov_b32_e32 v105, 0
	v_pk_mul_f32 v[106:107], v[100:101], v[168:169]
	v_mov_b32_e32 v108, 0
	v_mov_b32_e32 v109, 0
	v_mov_b32_dpp v104, v102 row_shr:1 row_mask:0xf bank_mask:0xf
	v_mov_b32_dpp v105, v103 row_shr:1 row_mask:0xf bank_mask:0xf
	v_mov_b32_dpp v108, v106 row_shr:1 row_mask:0xf bank_mask:0xf
	v_mov_b32_dpp v109, v107 row_shr:1 row_mask:0xf bank_mask:0xf
	v_pk_fma_f32 v[102:103], v[100:101], v[178:179], v[104:105]
	v_mov_b32_e32 v104, 0
	v_mov_b32_e32 v105, 0
	v_pk_fma_f32 v[106:107], v[100:101], v[168:169], v[108:109]
	v_mov_b32_e32 v108, 0
	v_mov_b32_e32 v109, 0
	v_mov_b32_dpp v104, v102 row_shr:2 row_mask:0xf bank_mask:0xf
	v_mov_b32_dpp v105, v103 row_shr:2 row_mask:0xf bank_mask:0xf
	v_mov_b32_dpp v108, v106 row_shr:2 row_mask:0xf bank_mask:0xf
	v_mov_b32_dpp v109, v107 row_shr:2 row_mask:0xf bank_mask:0xf
	v_pk_add_f32 v[102:103], v[102:103], v[104:105]
	v_mov_b32_e32 v104, 0
	v_mov_b32_e32 v105, 0
	v_pk_add_f32 v[106:107], v[106:107], v[108:109]
	v_mov_b32_e32 v108, 0
	v_mov_b32_e32 v109, 0
	v_mov_b32_dpp v104, v102 row_shr:4 row_mask:0xf bank_mask:0xf
	v_mov_b32_dpp v105, v103 row_shr:4 row_mask:0xf bank_mask:0xf
	v_mov_b32_dpp v108, v106 row_shr:4 row_mask:0xf bank_mask:0xf
	v_mov_b32_dpp v109, v107 row_shr:4 row_mask:0xf bank_mask:0xf
	v_pk_add_f32 v[102:103], v[102:103], v[104:105]
	v_mov_b32_e32 v104, 0
	v_mov_b32_e32 v105, 0
	v_pk_add_f32 v[106:107], v[106:107], v[108:109]
	v_mov_b32_e32 v108, 0
	v_mov_b32_e32 v109, 0
	v_mov_b32_dpp v104, v102 row_shr:8 row_mask:0xf bank_mask:0xf
	v_mov_b32_dpp v105, v103 row_shr:8 row_mask:0xf bank_mask:0xf
	v_mov_b32_dpp v108, v106 row_shr:8 row_mask:0xf bank_mask:0xf
	v_mov_b32_dpp v109, v107 row_shr:8 row_mask:0xf bank_mask:0xf
	s_and_saveexec_b64 s[24:25], s[6:7]
	v_pk_add_f32 v[106:107], v[106:107], v[108:109]
	v_pk_add_f32 v[104:105], v[102:103], v[104:105]
	ds_write_b128 v111, v[104:107] offset:320
	s_or_b64 exec, exec, s[24:25]
	v_pk_mul_f32 v[102:103], v[100:101], v[150:151]
	v_mov_b32_e32 v104, 0
	v_mov_b32_e32 v105, 0
	v_pk_mul_f32 v[106:107], v[100:101], v[140:141]
	v_mov_b32_e32 v108, 0
	v_mov_b32_e32 v109, 0
	v_mov_b32_dpp v104, v102 row_shr:1 row_mask:0xf bank_mask:0xf
	v_mov_b32_dpp v105, v103 row_shr:1 row_mask:0xf bank_mask:0xf
	v_mov_b32_dpp v108, v106 row_shr:1 row_mask:0xf bank_mask:0xf
	v_mov_b32_dpp v109, v107 row_shr:1 row_mask:0xf bank_mask:0xf
	v_pk_fma_f32 v[102:103], v[100:101], v[150:151], v[104:105]
	v_mov_b32_e32 v104, 0
	v_mov_b32_e32 v105, 0
	v_pk_fma_f32 v[106:107], v[100:101], v[140:141], v[108:109]
	v_mov_b32_e32 v108, 0
	v_mov_b32_e32 v109, 0
	v_mov_b32_dpp v104, v102 row_shr:2 row_mask:0xf bank_mask:0xf
	v_mov_b32_dpp v105, v103 row_shr:2 row_mask:0xf bank_mask:0xf
	v_mov_b32_dpp v108, v106 row_shr:2 row_mask:0xf bank_mask:0xf
	v_mov_b32_dpp v109, v107 row_shr:2 row_mask:0xf bank_mask:0xf
	v_pk_add_f32 v[102:103], v[102:103], v[104:105]
	v_mov_b32_e32 v104, 0
	v_mov_b32_e32 v105, 0
	v_pk_add_f32 v[106:107], v[106:107], v[108:109]
	v_mov_b32_e32 v108, 0
	v_mov_b32_e32 v109, 0
	v_mov_b32_dpp v104, v102 row_shr:4 row_mask:0xf bank_mask:0xf
	v_mov_b32_dpp v105, v103 row_shr:4 row_mask:0xf bank_mask:0xf
	v_mov_b32_dpp v108, v106 row_shr:4 row_mask:0xf bank_mask:0xf
	v_mov_b32_dpp v109, v107 row_shr:4 row_mask:0xf bank_mask:0xf
	v_pk_add_f32 v[102:103], v[102:103], v[104:105]
	v_mov_b32_e32 v104, 0
	v_mov_b32_e32 v105, 0
	v_pk_add_f32 v[106:107], v[106:107], v[108:109]
	v_mov_b32_e32 v108, 0
	v_mov_b32_e32 v109, 0
	v_mov_b32_dpp v104, v102 row_shr:8 row_mask:0xf bank_mask:0xf
	v_mov_b32_dpp v105, v103 row_shr:8 row_mask:0xf bank_mask:0xf
	v_mov_b32_dpp v108, v106 row_shr:8 row_mask:0xf bank_mask:0xf
	v_mov_b32_dpp v109, v107 row_shr:8 row_mask:0xf bank_mask:0xf
	s_and_saveexec_b64 s[24:25], s[6:7]
	v_pk_add_f32 v[106:107], v[106:107], v[108:109]
	v_pk_add_f32 v[104:105], v[102:103], v[104:105]
	ds_write_b128 v111, v[104:107] offset:384
	s_or_b64 exec, exec, s[24:25]
	v_pk_mul_f32 v[102:103], v[100:101], v[138:139]
	v_mov_b32_e32 v104, 0
	v_mov_b32_e32 v105, 0
	v_pk_mul_f32 v[106:107], v[100:101], v[136:137]
	v_mov_b32_e32 v108, 0
	v_mov_b32_e32 v109, 0
	v_mov_b32_dpp v104, v102 row_shr:1 row_mask:0xf bank_mask:0xf
	v_mov_b32_dpp v105, v103 row_shr:1 row_mask:0xf bank_mask:0xf
	v_mov_b32_dpp v108, v106 row_shr:1 row_mask:0xf bank_mask:0xf
	v_mov_b32_dpp v109, v107 row_shr:1 row_mask:0xf bank_mask:0xf
	v_pk_fma_f32 v[102:103], v[100:101], v[138:139], v[104:105]
	v_mov_b32_e32 v104, 0
	v_mov_b32_e32 v105, 0
	v_pk_fma_f32 v[100:101], v[100:101], v[136:137], v[108:109]
	v_mov_b32_e32 v106, 0
	v_mov_b32_e32 v107, 0
	v_mov_b32_dpp v104, v102 row_shr:2 row_mask:0xf bank_mask:0xf
	v_mov_b32_dpp v105, v103 row_shr:2 row_mask:0xf bank_mask:0xf
	v_mov_b32_dpp v106, v100 row_shr:2 row_mask:0xf bank_mask:0xf
	v_mov_b32_dpp v107, v101 row_shr:2 row_mask:0xf bank_mask:0xf
	v_pk_add_f32 v[102:103], v[102:103], v[104:105]
	v_mov_b32_e32 v104, 0
	v_mov_b32_e32 v105, 0
	v_pk_add_f32 v[100:101], v[100:101], v[106:107]
	v_mov_b32_e32 v106, 0
	v_mov_b32_e32 v107, 0
	v_mov_b32_dpp v104, v102 row_shr:4 row_mask:0xf bank_mask:0xf
	v_mov_b32_dpp v105, v103 row_shr:4 row_mask:0xf bank_mask:0xf
	v_mov_b32_dpp v106, v100 row_shr:4 row_mask:0xf bank_mask:0xf
	v_mov_b32_dpp v107, v101 row_shr:4 row_mask:0xf bank_mask:0xf
	v_pk_add_f32 v[102:103], v[102:103], v[104:105]
	v_mov_b32_e32 v104, 0
	v_mov_b32_e32 v105, 0
	v_pk_add_f32 v[100:101], v[100:101], v[106:107]
	v_mov_b32_e32 v106, 0
	v_mov_b32_e32 v107, 0
	v_mov_b32_dpp v104, v102 row_shr:8 row_mask:0xf bank_mask:0xf
	v_mov_b32_dpp v105, v103 row_shr:8 row_mask:0xf bank_mask:0xf
	v_mov_b32_dpp v106, v100 row_shr:8 row_mask:0xf bank_mask:0xf
	v_mov_b32_dpp v107, v101 row_shr:8 row_mask:0xf bank_mask:0xf
	s_and_saveexec_b64 s[24:25], s[6:7]
	v_pk_add_f32 v[106:107], v[100:101], v[106:107]
	v_pk_add_f32 v[104:105], v[102:103], v[104:105]
	ds_write_b128 v111, v[104:107] offset:448
	s_or_b64 exec, exec, s[24:25]
	s_and_saveexec_b64 s[24:25], s[4:5]
	v_add_f32_e32 v99, v110, v99
	v_mov_b32_e32 v100, s28
	ds_write_b64 v100, v[98:99] offset:512
	s_or_b64 exec, exec, s[24:25]
	v_mov_b32_e32 v218, 0xff800000
	v_mov_b32_e32 v219, 0
	v_mov_b32_e32 v198, 0
	v_mov_b32_e32 v199, 0
	v_mov_b32_e32 v196, 0
	v_mov_b32_e32 v197, 0
	v_mov_b32_e32 v194, 0
	v_mov_b32_e32 v195, 0
	v_mov_b32_e32 v192, 0
	v_mov_b32_e32 v193, 0
	v_mov_b32_e32 v190, 0
	v_mov_b32_e32 v191, 0
	v_mov_b32_e32 v188, 0
	v_mov_b32_e32 v189, 0
	v_mov_b32_e32 v186, 0
	v_mov_b32_e32 v187, 0
	v_mov_b32_e32 v184, 0
	v_mov_b32_e32 v185, 0
	v_mov_b32_e32 v182, 0
	v_mov_b32_e32 v183, 0
	v_mov_b32_e32 v180, 0
	v_mov_b32_e32 v181, 0
	v_mov_b32_e32 v178, 0
	v_mov_b32_e32 v179, 0
	v_mov_b32_e32 v168, 0
	v_mov_b32_e32 v169, 0
	v_mov_b32_e32 v150, 0
	v_mov_b32_e32 v151, 0
	v_mov_b32_e32 v140, 0
	v_mov_b32_e32 v141, 0
	v_mov_b32_e32 v138, 0
	v_mov_b32_e32 v139, 0
	v_mov_b32_e32 v136, 0
	v_mov_b32_e32 v137, 0
	s_waitcnt lgkmcnt(0)
	s_branch .Lp1_mfma

.Lp1_mfma:
	ds_read_b128 v[142:145], v214
	ds_read_b128 v[220:223], v211
	ds_read_b128 v[224:227], v211 offset:8704
	ds_read_b128 v[228:231], v211 offset:17408
	ds_read_b128 v[232:235], v211 offset:26112
	ds_read_b128 v[236:239], v211 offset:34816
	ds_read_b128 v[240:243], v211 offset:43520
	ds_read_b128 v[244:247], v211 offset:52224
	ds_read_b128 v[248:251], v211 offset:60928
	ds_read_b128 v[146:149], v214 offset:64
	v_or_b32_e32 v133, 0x22000, v203
	s_waitcnt lgkmcnt(8)
	v_mfma_f32_16x16x32_bf16 v[98:101], v[220:223], v[142:145], 0
	ds_read_b128 v[220:223], v211 offset:64
	s_waitcnt lgkmcnt(8)
	v_mfma_f32_16x16x32_bf16 v[102:105], v[224:227], v[142:145], 0
	ds_read_b128 v[224:227], v211 offset:8768
	s_waitcnt lgkmcnt(8)
	v_mfma_f32_16x16x32_bf16 v[106:109], v[228:231], v[142:145], 0
	ds_read_b128 v[228:231], v211 offset:17472
	s_waitcnt lgkmcnt(8)
	v_mfma_f32_16x16x32_bf16 v[110:113], v[232:235], v[142:145], 0
	ds_read_b128 v[232:235], v211 offset:26176
	s_waitcnt lgkmcnt(8)
	v_mfma_f32_16x16x32_bf16 v[114:117], v[236:239], v[142:145], 0
	ds_read_b128 v[236:239], v211 offset:34880
	s_waitcnt lgkmcnt(8)
	v_mfma_f32_16x16x32_bf16 v[118:121], v[240:243], v[142:145], 0
	ds_read_b128 v[240:243], v211 offset:43584
	s_waitcnt lgkmcnt(8)
	v_mfma_f32_16x16x32_bf16 v[122:125], v[244:247], v[142:145], 0
	ds_read_b128 v[244:247], v211 offset:52288
	s_waitcnt lgkmcnt(8)
	v_mfma_f32_16x16x32_bf16 v[126:129], v[248:251], v[142:145], 0
	ds_read_b128 v[248:251], v211 offset:60992
	ds_read_b128 v[142:145], v214 offset:128
	s_waitcnt lgkmcnt(8)
	v_mfma_f32_16x16x32_bf16 v[98:101], v[220:223], v[146:149], v[98:101]
	ds_read_b128 v[220:223], v211 offset:128
	s_waitcnt lgkmcnt(8)
	v_mfma_f32_16x16x32_bf16 v[102:105], v[224:227], v[146:149], v[102:105]
	ds_read_b128 v[224:227], v211 offset:8832
	s_waitcnt lgkmcnt(8)
	v_mfma_f32_16x16x32_bf16 v[106:109], v[228:231], v[146:149], v[106:109]
	ds_read_b128 v[228:231], v211 offset:17536
	s_waitcnt lgkmcnt(8)
	v_mfma_f32_16x16x32_bf16 v[110:113], v[232:235], v[146:149], v[110:113]
	ds_read_b128 v[232:235], v211 offset:26240
	s_waitcnt lgkmcnt(8)
	v_mfma_f32_16x16x32_bf16 v[114:117], v[236:239], v[146:149], v[114:117]
	ds_read_b128 v[236:239], v211 offset:34944
	s_waitcnt lgkmcnt(8)
	v_mfma_f32_16x16x32_bf16 v[118:121], v[240:243], v[146:149], v[118:121]
	ds_read_b128 v[240:243], v211 offset:43648
	s_waitcnt lgkmcnt(8)
	v_mfma_f32_16x16x32_bf16 v[122:125], v[244:247], v[146:149], v[122:125]
	ds_read_b128 v[244:247], v211 offset:52352
	s_waitcnt lgkmcnt(8)
	v_mfma_f32_16x16x32_bf16 v[126:129], v[248:251], v[146:149], v[126:129]
	ds_read_b128 v[248:251], v211 offset:61056
	ds_read_b128 v[146:149], v214 offset:192
	s_waitcnt lgkmcnt(8)
	v_mfma_f32_16x16x32_bf16 v[98:101], v[220:223], v[142:145], v[98:101]
	ds_read_b128 v[220:223], v211 offset:192
	s_waitcnt lgkmcnt(8)
	v_mfma_f32_16x16x32_bf16 v[102:105], v[224:227], v[142:145], v[102:105]
	ds_read_b128 v[224:227], v211 offset:8896
	s_waitcnt lgkmcnt(8)
	v_mfma_f32_16x16x32_bf16 v[106:109], v[228:231], v[142:145], v[106:109]
	ds_read_b128 v[228:231], v211 offset:17600
	s_waitcnt lgkmcnt(8)
	v_mfma_f32_16x16x32_bf16 v[110:113], v[232:235], v[142:145], v[110:113]
	ds_read_b128 v[232:235], v211 offset:26304
	s_waitcnt lgkmcnt(8)
	v_mfma_f32_16x16x32_bf16 v[114:117], v[236:239], v[142:145], v[114:117]
	ds_read_b128 v[236:239], v211 offset:35008
	s_waitcnt lgkmcnt(8)
	v_mfma_f32_16x16x32_bf16 v[118:121], v[240:243], v[142:145], v[118:121]
	ds_read_b128 v[240:243], v211 offset:43712
	s_waitcnt lgkmcnt(8)
	v_mfma_f32_16x16x32_bf16 v[122:125], v[244:247], v[142:145], v[122:125]
	ds_read_b128 v[244:247], v211 offset:52416
	s_waitcnt lgkmcnt(8)
	v_mfma_f32_16x16x32_bf16 v[126:129], v[248:251], v[142:145], v[126:129]
	ds_read_b128 v[248:251], v211 offset:61120
	ds_read_b128 v[142:145], v214 offset:256
	s_waitcnt lgkmcnt(8)
	v_mfma_f32_16x16x32_bf16 v[98:101], v[220:223], v[146:149], v[98:101]
	ds_read_b128 v[220:223], v211 offset:256
	s_waitcnt lgkmcnt(8)
	v_mfma_f32_16x16x32_bf16 v[102:105], v[224:227], v[146:149], v[102:105]
	ds_read_b128 v[224:227], v211 offset:8960
	s_waitcnt lgkmcnt(8)
	v_mfma_f32_16x16x32_bf16 v[106:109], v[228:231], v[146:149], v[106:109]
	ds_read_b128 v[228:231], v211 offset:17664
	s_waitcnt lgkmcnt(8)
	v_mfma_f32_16x16x32_bf16 v[110:113], v[232:235], v[146:149], v[110:113]
	ds_read_b128 v[232:235], v211 offset:26368
	s_waitcnt lgkmcnt(8)
	v_mfma_f32_16x16x32_bf16 v[114:117], v[236:239], v[146:149], v[114:117]
	ds_read_b128 v[236:239], v211 offset:35072
	s_waitcnt lgkmcnt(8)
	v_mfma_f32_16x16x32_bf16 v[118:121], v[240:243], v[146:149], v[118:121]
	ds_read_b128 v[240:243], v211 offset:43776
	s_waitcnt lgkmcnt(8)
	v_mfma_f32_16x16x32_bf16 v[122:125], v[244:247], v[146:149], v[122:125]
	ds_read_b128 v[244:247], v211 offset:52480
	s_waitcnt lgkmcnt(8)
	v_mfma_f32_16x16x32_bf16 v[126:129], v[248:251], v[146:149], v[126:129]
	ds_read_b128 v[248:251], v211 offset:61184
	ds_read_b128 v[146:149], v214 offset:320
	s_waitcnt lgkmcnt(8)
	v_mfma_f32_16x16x32_bf16 v[98:101], v[220:223], v[142:145], v[98:101]
	ds_read_b128 v[220:223], v211 offset:320
	s_waitcnt lgkmcnt(8)
	v_mfma_f32_16x16x32_bf16 v[102:105], v[224:227], v[142:145], v[102:105]
	ds_read_b128 v[224:227], v211 offset:9024
	s_waitcnt lgkmcnt(8)
	v_mfma_f32_16x16x32_bf16 v[106:109], v[228:231], v[142:145], v[106:109]
	ds_read_b128 v[228:231], v211 offset:17728
	s_waitcnt lgkmcnt(8)
	v_mfma_f32_16x16x32_bf16 v[110:113], v[232:235], v[142:145], v[110:113]
	ds_read_b128 v[232:235], v211 offset:26432
	s_waitcnt lgkmcnt(8)
	v_mfma_f32_16x16x32_bf16 v[114:117], v[236:239], v[142:145], v[114:117]
	ds_read_b128 v[236:239], v211 offset:35136
	s_waitcnt lgkmcnt(8)
	v_mfma_f32_16x16x32_bf16 v[118:121], v[240:243], v[142:145], v[118:121]
	ds_read_b128 v[240:243], v211 offset:43840
	s_waitcnt lgkmcnt(8)
	v_mfma_f32_16x16x32_bf16 v[122:125], v[244:247], v[142:145], v[122:125]
	ds_read_b128 v[244:247], v211 offset:52544
	s_waitcnt lgkmcnt(8)
	v_mfma_f32_16x16x32_bf16 v[126:129], v[248:251], v[142:145], v[126:129]
	ds_read_b128 v[248:251], v211 offset:61248
	ds_read_b128 v[142:145], v214 offset:384
	s_waitcnt lgkmcnt(8)
	v_mfma_f32_16x16x32_bf16 v[98:101], v[220:223], v[146:149], v[98:101]
	ds_read_b128 v[220:223], v211 offset:384
	s_waitcnt lgkmcnt(8)
	v_mfma_f32_16x16x32_bf16 v[102:105], v[224:227], v[146:149], v[102:105]
	ds_read_b128 v[224:227], v211 offset:9088
	s_waitcnt lgkmcnt(8)
	v_mfma_f32_16x16x32_bf16 v[106:109], v[228:231], v[146:149], v[106:109]
	ds_read_b128 v[228:231], v211 offset:17792
	s_waitcnt lgkmcnt(8)
	v_mfma_f32_16x16x32_bf16 v[110:113], v[232:235], v[146:149], v[110:113]
	ds_read_b128 v[232:235], v211 offset:26496
	s_waitcnt lgkmcnt(8)
	v_mfma_f32_16x16x32_bf16 v[114:117], v[236:239], v[146:149], v[114:117]
	ds_read_b128 v[236:239], v211 offset:35200
	s_waitcnt lgkmcnt(8)
	v_mfma_f32_16x16x32_bf16 v[118:121], v[240:243], v[146:149], v[118:121]
	ds_read_b128 v[240:243], v211 offset:43904
	s_waitcnt lgkmcnt(8)
	v_mfma_f32_16x16x32_bf16 v[122:125], v[244:247], v[146:149], v[122:125]
	ds_read_b128 v[244:247], v211 offset:52608
	s_waitcnt lgkmcnt(8)
	v_mfma_f32_16x16x32_bf16 v[126:129], v[248:251], v[146:149], v[126:129]
	ds_read_b128 v[248:251], v211 offset:61312
	ds_read_b128 v[146:149], v214 offset:448
	s_waitcnt lgkmcnt(8)
	v_mfma_f32_16x16x32_bf16 v[98:101], v[220:223], v[142:145], v[98:101]
	ds_read_b128 v[220:223], v211 offset:448
	s_waitcnt lgkmcnt(8)
	v_mfma_f32_16x16x32_bf16 v[102:105], v[224:227], v[142:145], v[102:105]
	ds_read_b128 v[224:227], v211 offset:9152
	s_waitcnt lgkmcnt(8)
	v_mfma_f32_16x16x32_bf16 v[106:109], v[228:231], v[142:145], v[106:109]
	ds_read_b128 v[228:231], v211 offset:17856
	s_waitcnt lgkmcnt(8)
	v_mfma_f32_16x16x32_bf16 v[110:113], v[232:235], v[142:145], v[110:113]
	ds_read_b128 v[232:235], v211 offset:26560
	s_waitcnt lgkmcnt(8)
	v_mfma_f32_16x16x32_bf16 v[114:117], v[236:239], v[142:145], v[114:117]
	ds_read_b128 v[236:239], v211 offset:35264
	s_waitcnt lgkmcnt(8)
	v_mfma_f32_16x16x32_bf16 v[118:121], v[240:243], v[142:145], v[118:121]
	ds_read_b128 v[240:243], v211 offset:43968
	s_waitcnt lgkmcnt(8)
	v_mfma_f32_16x16x32_bf16 v[122:125], v[244:247], v[142:145], v[122:125]
	ds_read_b128 v[244:247], v211 offset:52672
	s_waitcnt lgkmcnt(8)
	v_mfma_f32_16x16x32_bf16 v[126:129], v[248:251], v[142:145], v[126:129]
	ds_read_b128 v[248:251], v211 offset:61376
	s_waitcnt lgkmcnt(7)
	v_mfma_f32_16x16x32_bf16 v[98:101], v[220:223], v[146:149], v[98:101]
	ds_read_b128 v[220:223], v133
	ds_read_b128 v[152:155], v133 offset:512
	s_waitcnt lgkmcnt(8)
	v_mfma_f32_16x16x32_bf16 v[102:105], v[224:227], v[146:149], v[102:105]
	ds_read_b128 v[224:227], v133 offset:64
	ds_read_b128 v[156:159], v133 offset:576
	s_waitcnt lgkmcnt(9)
	v_mfma_f32_16x16x32_bf16 v[106:109], v[228:231], v[146:149], v[106:109]
	ds_read_b128 v[228:231], v133 offset:128
	ds_read_b128 v[160:163], v133 offset:640
	s_waitcnt lgkmcnt(10)
	v_mfma_f32_16x16x32_bf16 v[110:113], v[232:235], v[146:149], v[110:113]
	ds_read_b128 v[232:235], v133 offset:192
	ds_read_b128 v[164:167], v133 offset:704
	s_waitcnt lgkmcnt(11)
	v_mfma_f32_16x16x32_bf16 v[114:117], v[236:239], v[146:149], v[114:117]
	ds_read_b128 v[236:239], v133 offset:256
	ds_read_b128 v[170:173], v133 offset:768
	s_waitcnt lgkmcnt(12)
	v_mfma_f32_16x16x32_bf16 v[118:121], v[240:243], v[146:149], v[118:121]
	ds_read_b128 v[240:243], v133 offset:320
	ds_read_b128 v[174:177], v133 offset:832
	s_waitcnt lgkmcnt(13)
	v_mfma_f32_16x16x32_bf16 v[122:125], v[244:247], v[146:149], v[122:125]
	ds_read_b128 v[244:247], v133 offset:384
	ds_read_b128 v[142:145], v133 offset:896
	s_waitcnt lgkmcnt(14)
	v_mfma_f32_16x16x32_bf16 v[126:129], v[248:251], v[146:149], v[126:129]
	s_waitcnt lgkmcnt(13)
	ds_read_b128 v[248:251], v133 offset:448
	ds_read_b128 v[252:255], v133 offset:960
	v_fmac_f32_e32 v220, 0x4038aa3b, v98
	v_fmac_f32_e32 v221, 0x4038aa3b, v99
	v_fmac_f32_e32 v222, 0x4038aa3b, v100
	v_fmac_f32_e32 v223, 0x4038aa3b, v101
	v_exp_f32_e32 v220, v220
	v_exp_f32_e32 v221, v221
	v_exp_f32_e32 v222, v222
	v_exp_f32_e32 v223, v223
	v_add_f32_e32 v220, 1.0, v220
	v_add_f32_e32 v221, 1.0, v221
	v_add_f32_e32 v222, 1.0, v222
	v_add_f32_e32 v223, 1.0, v223
	v_rcp_f32_e32 v98, v220
	v_rcp_f32_e32 v99, v221
	v_rcp_f32_e32 v100, v222
	v_rcp_f32_e32 v101, v223
	s_waitcnt lgkmcnt(14)
	v_mul_f32_e32 v146, v152, v98
	v_fmac_f32_e32 v146, v153, v99
	v_fmac_f32_e32 v146, v154, v100
	v_fmac_f32_e32 v146, v155, v101
	s_waitcnt lgkmcnt(13)
	v_fmac_f32_e32 v224, 0x4038aa3b, v102
	v_fmac_f32_e32 v225, 0x4038aa3b, v103
	v_fmac_f32_e32 v226, 0x4038aa3b, v104
	v_fmac_f32_e32 v227, 0x4038aa3b, v105
	v_exp_f32_e32 v224, v224
	v_exp_f32_e32 v225, v225
	v_exp_f32_e32 v226, v226
	v_exp_f32_e32 v227, v227
	v_add_f32_e32 v224, 1.0, v224
	v_add_f32_e32 v225, 1.0, v225
	v_add_f32_e32 v226, 1.0, v226
	v_add_f32_e32 v227, 1.0, v227
	v_rcp_f32_e32 v102, v224
	v_rcp_f32_e32 v103, v225
	v_rcp_f32_e32 v104, v226
	v_rcp_f32_e32 v105, v227
	s_waitcnt lgkmcnt(12)
	v_fmac_f32_e32 v146, v156, v102
	v_fmac_f32_e32 v146, v157, v103
	v_fmac_f32_e32 v146, v158, v104
	v_fmac_f32_e32 v146, v159, v105
	s_waitcnt lgkmcnt(11)
	v_fmac_f32_e32 v228, 0x4038aa3b, v106
	v_fmac_f32_e32 v229, 0x4038aa3b, v107
	v_fmac_f32_e32 v230, 0x4038aa3b, v108
	v_fmac_f32_e32 v231, 0x4038aa3b, v109
	v_exp_f32_e32 v228, v228
	v_exp_f32_e32 v229, v229
	v_exp_f32_e32 v230, v230
	v_exp_f32_e32 v231, v231
	v_add_f32_e32 v228, 1.0, v228
	v_add_f32_e32 v229, 1.0, v229
	v_add_f32_e32 v230, 1.0, v230
	v_add_f32_e32 v231, 1.0, v231
	v_rcp_f32_e32 v106, v228
	v_rcp_f32_e32 v107, v229
	v_rcp_f32_e32 v108, v230
	v_rcp_f32_e32 v109, v231
	s_waitcnt lgkmcnt(10)
	v_fmac_f32_e32 v146, v160, v106
	v_fmac_f32_e32 v146, v161, v107
	v_fmac_f32_e32 v146, v162, v108
	v_fmac_f32_e32 v146, v163, v109
	s_waitcnt lgkmcnt(9)
	v_fmac_f32_e32 v232, 0x4038aa3b, v110
	v_fmac_f32_e32 v233, 0x4038aa3b, v111
	v_fmac_f32_e32 v234, 0x4038aa3b, v112
	v_fmac_f32_e32 v235, 0x4038aa3b, v113
	v_exp_f32_e32 v232, v232
	v_exp_f32_e32 v233, v233
	v_exp_f32_e32 v234, v234
	v_exp_f32_e32 v235, v235
	v_add_f32_e32 v232, 1.0, v232
	v_add_f32_e32 v233, 1.0, v233
	v_add_f32_e32 v234, 1.0, v234
	v_add_f32_e32 v235, 1.0, v235
	v_rcp_f32_e32 v110, v232
	v_rcp_f32_e32 v111, v233
	v_rcp_f32_e32 v112, v234
	v_rcp_f32_e32 v113, v235
	s_waitcnt lgkmcnt(8)
	v_fmac_f32_e32 v146, v164, v110
	v_fmac_f32_e32 v146, v165, v111
	v_fmac_f32_e32 v146, v166, v112
	v_fmac_f32_e32 v146, v167, v113
	s_waitcnt lgkmcnt(7)
	v_fmac_f32_e32 v236, 0x4038aa3b, v114
	v_fmac_f32_e32 v237, 0x4038aa3b, v115
	v_fmac_f32_e32 v238, 0x4038aa3b, v116
	v_fmac_f32_e32 v239, 0x4038aa3b, v117
	v_exp_f32_e32 v236, v236
	v_exp_f32_e32 v237, v237
	v_exp_f32_e32 v238, v238
	v_exp_f32_e32 v239, v239
	v_add_f32_e32 v236, 1.0, v236
	v_add_f32_e32 v237, 1.0, v237
	v_add_f32_e32 v238, 1.0, v238
	v_add_f32_e32 v239, 1.0, v239
	v_rcp_f32_e32 v114, v236
	v_rcp_f32_e32 v115, v237
	v_rcp_f32_e32 v116, v238
	v_rcp_f32_e32 v117, v239
	s_waitcnt lgkmcnt(6)
	v_fmac_f32_e32 v146, v170, v114
	v_fmac_f32_e32 v146, v171, v115
	v_fmac_f32_e32 v146, v172, v116
	v_fmac_f32_e32 v146, v173, v117
	s_waitcnt lgkmcnt(5)
	v_fmac_f32_e32 v240, 0x4038aa3b, v118
	v_fmac_f32_e32 v241, 0x4038aa3b, v119
	v_fmac_f32_e32 v242, 0x4038aa3b, v120
	v_fmac_f32_e32 v243, 0x4038aa3b, v121
	v_exp_f32_e32 v240, v240
	v_exp_f32_e32 v241, v241
	v_exp_f32_e32 v242, v242
	v_exp_f32_e32 v243, v243
	v_add_f32_e32 v240, 1.0, v240
	v_add_f32_e32 v241, 1.0, v241
	v_add_f32_e32 v242, 1.0, v242
	v_add_f32_e32 v243, 1.0, v243
	v_rcp_f32_e32 v118, v240
	v_rcp_f32_e32 v119, v241
	v_rcp_f32_e32 v120, v242
	v_rcp_f32_e32 v121, v243
	s_waitcnt lgkmcnt(4)
	v_fmac_f32_e32 v146, v174, v118
	v_fmac_f32_e32 v146, v175, v119
	v_fmac_f32_e32 v146, v176, v120
	v_fmac_f32_e32 v146, v177, v121
	s_waitcnt lgkmcnt(3)
	v_fmac_f32_e32 v244, 0x4038aa3b, v122
	v_fmac_f32_e32 v245, 0x4038aa3b, v123
	v_fmac_f32_e32 v246, 0x4038aa3b, v124
	v_fmac_f32_e32 v247, 0x4038aa3b, v125
	v_exp_f32_e32 v244, v244
	v_exp_f32_e32 v245, v245
	v_exp_f32_e32 v246, v246
	v_exp_f32_e32 v247, v247
	v_add_f32_e32 v244, 1.0, v244
	v_add_f32_e32 v245, 1.0, v245
	v_add_f32_e32 v246, 1.0, v246
	v_add_f32_e32 v247, 1.0, v247
	v_rcp_f32_e32 v122, v244
	v_rcp_f32_e32 v123, v245
	v_rcp_f32_e32 v124, v246
	v_rcp_f32_e32 v125, v247
	s_waitcnt lgkmcnt(2)
	v_fmac_f32_e32 v146, v142, v122
	v_fmac_f32_e32 v146, v143, v123
	v_fmac_f32_e32 v146, v144, v124
	v_fmac_f32_e32 v146, v145, v125
	s_waitcnt lgkmcnt(1)
	v_fmac_f32_e32 v248, 0x4038aa3b, v126
	v_fmac_f32_e32 v249, 0x4038aa3b, v127
	v_fmac_f32_e32 v250, 0x4038aa3b, v128
	v_fmac_f32_e32 v251, 0x4038aa3b, v129
	v_exp_f32_e32 v248, v248
	v_exp_f32_e32 v249, v249
	v_exp_f32_e32 v250, v250
	v_exp_f32_e32 v251, v251
	v_add_f32_e32 v248, 1.0, v248
	v_add_f32_e32 v249, 1.0, v249
	v_add_f32_e32 v250, 1.0, v250
	v_add_f32_e32 v251, 1.0, v251
	v_rcp_f32_e32 v126, v248
	v_rcp_f32_e32 v127, v249
	v_rcp_f32_e32 v128, v250
	v_rcp_f32_e32 v129, v251
	s_waitcnt lgkmcnt(0)
	v_fmac_f32_e32 v146, v252, v126
	v_fmac_f32_e32 v146, v253, v127
	v_fmac_f32_e32 v146, v254, v128
	v_fmac_f32_e32 v146, v255, v129
	ds_bpermute_b32 v147, v201, v146
	s_waitcnt lgkmcnt(0)
	v_add_f32_e32 v146, v146, v147
	ds_bpermute_b32 v147, v200, v146
	s_waitcnt lgkmcnt(0)
	v_add_f32_e32 v146, v146, v147
	v_fmamk_f32 v147, v146, 0xc038aa3b, v210
	v_max_f32_e32 v148, v218, v147
	v_sub_f32_e32 v146, v218, v148
	v_sub_f32_e32 v147, v147, v148
	v_mov_b32_e32 v218, v148
	v_exp_f32_e32 v146, v146
	v_exp_f32_e32 v148, v147
	s_nop 1
	v_fma_f32 v219, v219, v146, v148
	v_pk_mul_f32 v[98:99], v[98:99], v[148:149] op_sel_hi:[1,0]
	v_pk_mul_f32 v[100:101], v[100:101], v[148:149] op_sel_hi:[1,0]
	v_pk_mul_f32 v[102:103], v[102:103], v[148:149] op_sel_hi:[1,0]
	v_pk_mul_f32 v[104:105], v[104:105], v[148:149] op_sel_hi:[1,0]
	v_pk_mul_f32 v[106:107], v[106:107], v[148:149] op_sel_hi:[1,0]
	v_pk_mul_f32 v[108:109], v[108:109], v[148:149] op_sel_hi:[1,0]
	v_pk_mul_f32 v[110:111], v[110:111], v[148:149] op_sel_hi:[1,0]
	v_pk_mul_f32 v[112:113], v[112:113], v[148:149] op_sel_hi:[1,0]
	v_pk_mul_f32 v[114:115], v[114:115], v[148:149] op_sel_hi:[1,0]
	v_pk_mul_f32 v[116:117], v[116:117], v[148:149] op_sel_hi:[1,0]
	v_pk_mul_f32 v[118:119], v[118:119], v[148:149] op_sel_hi:[1,0]
	v_pk_mul_f32 v[120:121], v[120:121], v[148:149] op_sel_hi:[1,0]
	v_pk_mul_f32 v[122:123], v[122:123], v[148:149] op_sel_hi:[1,0]
	v_pk_mul_f32 v[124:125], v[124:125], v[148:149] op_sel_hi:[1,0]
	v_pk_mul_f32 v[126:127], v[126:127], v[148:149] op_sel_hi:[1,0]
	v_pk_mul_f32 v[128:129], v[128:129], v[148:149] op_sel_hi:[1,0]
	v_pk_fma_f32 v[198:199], v[198:199], v[146:147], v[98:99] op_sel_hi:[1,0,1]
	v_pk_fma_f32 v[196:197], v[196:197], v[146:147], v[100:101] op_sel_hi:[1,0,1]
	v_pk_fma_f32 v[194:195], v[194:195], v[146:147], v[102:103] op_sel_hi:[1,0,1]
	v_pk_fma_f32 v[192:193], v[192:193], v[146:147], v[104:105] op_sel_hi:[1,0,1]
	v_pk_fma_f32 v[190:191], v[190:191], v[146:147], v[106:107] op_sel_hi:[1,0,1]
	v_pk_fma_f32 v[188:189], v[188:189], v[146:147], v[108:109] op_sel_hi:[1,0,1]
	v_pk_fma_f32 v[186:187], v[186:187], v[146:147], v[110:111] op_sel_hi:[1,0,1]
	v_pk_fma_f32 v[184:185], v[184:185], v[146:147], v[112:113] op_sel_hi:[1,0,1]
	v_pk_fma_f32 v[182:183], v[182:183], v[146:147], v[114:115] op_sel_hi:[1,0,1]
	v_pk_fma_f32 v[180:181], v[180:181], v[146:147], v[116:117] op_sel_hi:[1,0,1]
	v_pk_fma_f32 v[178:179], v[178:179], v[146:147], v[118:119] op_sel_hi:[1,0,1]
	v_pk_fma_f32 v[168:169], v[168:169], v[146:147], v[120:121] op_sel_hi:[1,0,1]
	v_pk_fma_f32 v[150:151], v[150:151], v[146:147], v[122:123] op_sel_hi:[1,0,1]
	v_pk_fma_f32 v[140:141], v[140:141], v[146:147], v[124:125] op_sel_hi:[1,0,1]
	v_pk_fma_f32 v[138:139], v[138:139], v[146:147], v[126:127] op_sel_hi:[1,0,1]
	v_pk_fma_f32 v[136:137], v[136:137], v[146:147], v[128:129] op_sel_hi:[1,0,1]
	s_cmpk_lt_i32 s26, 0x80
	s_cbranch_scc0 .LBB0_40
	s_mov_b32 s34, s27
	s_mov_b32 s35, s26
	s_branch .LBB0_9

	.amdhsa_kernel _Z12pool1_kernelPKfS0_S0_S0_S0_S0_S0_S0_S0_S0_PfS1_
		.amdhsa_group_segment_fixed_size 161344
		.amdhsa_private_segment_fixed_size 0
		.amdhsa_kernarg_size 96
		.amdhsa_user_sgpr_count 2
		.amdhsa_user_sgpr_dispatch_ptr 0
		.amdhsa_user_sgpr_queue_ptr 0
		.amdhsa_user_sgpr_kernarg_segment_ptr 1
		.amdhsa_user_sgpr_dispatch_id 0
		.amdhsa_user_sgpr_kernarg_preload_length 0
		.amdhsa_user_sgpr_kernarg_preload_offset 0
		.amdhsa_user_sgpr_private_segment_size 0
		.amdhsa_uses_dynamic_stack 0
		.amdhsa_enable_private_segment 0
		.amdhsa_system_sgpr_workgroup_id_x 1
		.amdhsa_system_sgpr_workgroup_id_y 0
		.amdhsa_system_sgpr_workgroup_id_z 0
		.amdhsa_system_sgpr_workgroup_info 0
		.amdhsa_system_vgpr_workitem_id 0
		.amdhsa_next_free_vgpr 256
		.amdhsa_next_free_sgpr 96
		.amdhsa_accum_offset 256
		.amdhsa_reserve_vcc 1
		.amdhsa_float_round_mode_32 0
		.amdhsa_float_round_mode_16_64 0
		.amdhsa_float_denorm_mode_32 3
		.amdhsa_float_denorm_mode_16_64 3
		.amdhsa_dx10_clamp 1
		.amdhsa_ieee_mode 1
		.amdhsa_fp16_overflow 0
		.amdhsa_tg_split 0
		.amdhsa_exception_fp_ieee_invalid_op 0
		.amdhsa_exception_fp_denorm_src 0
		.amdhsa_exception_fp_ieee_div_zero 0
		.amdhsa_exception_fp_ieee_overflow 0
		.amdhsa_exception_fp_ieee_underflow 0
		.amdhsa_exception_fp_ieee_inexact 0
		.amdhsa_exception_int_div_zero 0
	.end_amdhsa_kernel

.Lfunc_end0:
	.size	_Z12pool1_kernelPKfS0_S0_S0_S0_S0_S0_S0_S0_S0_PfS1_, .Lfunc_end0-_Z12pool1_kernelPKfS0_S0_S0_S0_S0_S0_S0_S0_S0_PfS1_
	.set _Z12pool1_kernelPKfS0_S0_S0_S0_S0_S0_S0_S0_S0_PfS1_.num_vgpr, 256
	.set _Z12pool1_kernelPKfS0_S0_S0_S0_S0_S0_S0_S0_S0_PfS1_.num_agpr, 0
	.set _Z12pool1_kernelPKfS0_S0_S0_S0_S0_S0_S0_S0_S0_PfS1_.numbered_sgpr, 36
	.set _Z12pool1_kernelPKfS0_S0_S0_S0_S0_S0_S0_S0_S0_PfS1_.num_named_barrier, 0
	.set _Z12pool1_kernelPKfS0_S0_S0_S0_S0_S0_S0_S0_S0_PfS1_.private_seg_size, 0
	.set _Z12pool1_kernelPKfS0_S0_S0_S0_S0_S0_S0_S0_S0_PfS1_.uses_vcc, 1
	.set _Z12pool1_kernelPKfS0_S0_S0_S0_S0_S0_S0_S0_S0_PfS1_.uses_flat_scratch, 0
	.set _Z12pool1_kernelPKfS0_S0_S0_S0_S0_S0_S0_S0_S0_PfS1_.has_dyn_sized_stack, 0
	.set _Z12pool1_kernelPKfS0_S0_S0_S0_S0_S0_S0_S0_S0_PfS1_.has_recursion, 0
	.set _Z12pool1_kernelPKfS0_S0_S0_S0_S0_S0_S0_S0_S0_PfS1_.has_indirect_call, 0

amdhsa.kernels:
  - .agpr_count:     0
    .args:
      - .actual_access:  read_only
        .address_space:  global
        .offset:         0
        .size:           8
        .value_kind:     global_buffer
      - .actual_access:  read_only
        .address_space:  global
        .offset:         8
        .size:           8
        .value_kind:     global_buffer
      - .actual_access:  read_only
        .address_space:  global
        .offset:         16
        .size:           8
        .value_kind:     global_buffer
      - .actual_access:  read_only
        .address_space:  global
        .offset:         24
        .size:           8
        .value_kind:     global_buffer
      - .actual_access:  read_only
        .address_space:  global
        .offset:         32
        .size:           8
        .value_kind:     global_buffer
      - .actual_access:  read_only
        .address_space:  global
        .offset:         40
        .size:           8
        .value_kind:     global_buffer
      - .actual_access:  read_only
        .address_space:  global
        .offset:         48
        .size:           8
        .value_kind:     global_buffer
      - .actual_access:  read_only
        .address_space:  global
        .offset:         56
        .size:           8
        .value_kind:     global_buffer
      - .actual_access:  read_only
        .address_space:  global
        .offset:         64
        .size:           8
        .value_kind:     global_buffer
      - .actual_access:  read_only
        .address_space:  global
        .offset:         72
        .size:           8
        .value_kind:     global_buffer
      - .actual_access:  write_only
        .address_space:  global
        .offset:         80
        .size:           8
        .value_kind:     global_buffer
      - .actual_access:  write_only
        .address_space:  global
        .offset:         88
        .size:           8
        .value_kind:     global_buffer
    .group_segment_fixed_size: 161344
    .kernarg_segment_align: 8
    .kernarg_segment_size: 96
    .language:       OpenCL C
    .language_version:
      - 2
      - 0
    .max_flat_workgroup_size: 512
    .name:           _Z12pool1_kernelPKfS0_S0_S0_S0_S0_S0_S0_S0_S0_PfS1_
    .private_segment_fixed_size: 0
    .sgpr_count:     42
    .sgpr_spill_count: 0
    .symbol:         _Z12pool1_kernelPKfS0_S0_S0_S0_S0_S0_S0_S0_S0_PfS1_.kd
    .uniform_work_group_size: 1
    .uses_dynamic_stack: false
    .vgpr_count:     256
    .vgpr_spill_count: 0
    .wavefront_size: 64
  - .agpr_count:     0
    .args:
      - .actual_access:  read_only
        .address_space:  global
        .offset:         0
        .size:           8
        .value_kind:     global_buffer
      - .actual_access:  read_only
        .address_space:  global
        .offset:         8
        .size:           8
        .value_kind:     global_buffer
      - .address_space:  global
        .offset:         16
        .size:           8
        .value_kind:     global_buffer
    .group_segment_fixed_size: 18592
    .kernarg_segment_align: 8
    .kernarg_segment_size: 24
    .language:       OpenCL C
    .language_version:
      - 2
      - 0
    .max_flat_workgroup_size: 256
    .name:           _Z12pool3_kernelPKfS0_Pf
    .private_segment_fixed_size: 0
    .sgpr_count:     16
    .sgpr_spill_count: 0
    .symbol:         _Z12pool3_kernelPKfS0_Pf.kd
    .uniform_work_group_size: 1
    .uses_dynamic_stack: false
    .vgpr_count:     40
    .vgpr_spill_count: 0
    .wavefront_size: 64
